# v43
# baseline (speedup 1.0000x reference)
.LBB0_34:
	s_or_b64 exec, exec, s[10:11]
	ds_read_b128 v[18:21], v72
	s_waitcnt vmcnt(3)
	v_cvt_pk_f16_f32 v14, v14, v15
	v_cvt_pk_f16_f32 v15, v16, v17
	v_cvt_pk_f16_f32 v16, v10, v11
	ds_read_b128 v[22:25], v71 offset:41984
	v_cvt_pk_f16_f32 v17, v12, v13
	ds_read_b128 v[10:13], v72 offset:1024
	ds_read_b128 v[26:29], v71 offset:42048
	s_waitcnt vmcnt(1)
	v_cvt_pk_f16_f32 v0, v6, v7
	v_cvt_pk_f16_f32 v1, v8, v9
	v_cvt_pk_f16_f32 v2, v2, v3
	s_waitcnt lgkmcnt(2)
	v_mfma_f32_16x16x32_f16 v[30:33], v[18:21], v[14:17], v[22:25]
	v_cvt_pk_f16_f32 v3, v4, v5
	s_add_i32 s10, s20, s12
	s_nop 0
	v_mfma_f32_16x16x32_f16 v[18:21], v[18:21], v[0:3], v[22:25]
	ds_read_b128 v[4:7], v72 offset:2048
	s_nop 1
	ds_read_b128 v[22:25], v71 offset:42112
	s_waitcnt lgkmcnt(2)
	v_exp_f32_e32 v78, v30
	v_mfma_f32_16x16x32_f16 v[34:37], v[10:13], v[14:17], v[26:29]
	v_exp_f32_e32 v79, v31
	v_exp_f32_e32 v20, v20
	v_mfma_f32_16x16x32_f16 v[8:11], v[10:13], v[0:3], v[26:29]
	ds_read_b128 v[44:47], v71 offset:42176
	s_nop 3
	v_exp_f32_e64 v80, v34 clamp
	v_exp_f32_e64 v81, v35 clamp
	ds_read_b128 v[26:29], v72 offset:3072
	s_waitcnt lgkmcnt(2)
	v_mfma_f32_16x16x32_f16 v[48:51], v[4:7], v[14:17], v[22:25]
	v_exp_f32_e64 v82, v36 clamp
	v_exp_f32_e64 v83, v37 clamp
	v_exp_f32_e32 v21, v21
	v_mfma_f32_16x16x32_f16 v[22:25], v[4:7], v[0:3], v[22:25]
	ds_read_b128 v[52:55], v72 offset:4096
	ds_read_b128 v[56:59], v71 offset:42240
	s_nop 1
	v_exp_f32_e32 v4, v48
	s_waitcnt lgkmcnt(2)
	v_mfma_f32_16x16x32_f16 v[60:63], v[26:29], v[14:17], v[44:47]
	v_exp_f32_e32 v5, v49
	v_exp_f32_e32 v48, v32
	v_exp_f32_e32 v49, v33
	v_mfma_f32_16x16x32_f16 v[26:29], v[26:29], v[0:3], v[44:47]
	ds_read_b128 v[64:67], v71 offset:42304
	v_exp_f32_e32 v6, v50
	v_exp_f32_e32 v7, v51
	ds_read_b128 v[44:47], v72 offset:5120
	s_waitcnt lgkmcnt(2)
	v_mfma_f32_16x16x32_f16 v[74:77], v[52:55], v[14:17], v[56:59]
	v_exp_f32_e32 v50, v18
	v_exp_f32_e32 v51, v19
	v_exp_f32_e32 v26, v26
	v_mfma_f32_16x16x32_f16 v[30:33], v[52:55], v[0:3], v[56:59]
	v_exp_f32_e64 v52, v8 clamp
	v_exp_f32_e64 v53, v9 clamp
	v_exp_f32_e32 v8, v22
	s_waitcnt lgkmcnt(0)
	v_mfma_f32_16x16x32_f16 v[34:37], v[44:47], v[14:17], v[64:67]
	v_exp_f32_e32 v9, v23
	v_exp_f32_e64 v22, v10 clamp
	v_exp_f32_e64 v23, v11 clamp
	v_mfma_f32_16x16x32_f16 v[44:47], v[44:47], v[0:3], v[64:67]
	v_exp_f32_e32 v10, v24
	v_exp_f32_e32 v11, v25
	v_exp_f32_e32 v24, v60
	v_exp_f32_e32 v25, v61
	v_exp_f32_e32 v12, v34
	v_exp_f32_e32 v13, v35
	v_exp_f32_e32 v18, v36
	v_exp_f32_e64 v54, v74 clamp
	v_exp_f32_e64 v55, v75 clamp
	v_exp_f32_e32 v34, v62
	v_exp_f32_e32 v35, v63
	v_exp_f32_e64 v56, v76 clamp
	v_exp_f32_e64 v57, v77 clamp
	v_exp_f32_e32 v19, v37
	v_exp_f32_e32 v27, v27
	v_exp_f32_e64 v30, v30 clamp
	v_exp_f32_e64 v31, v31 clamp
	v_exp_f32_e32 v36, v44
	v_exp_f32_e32 v37, v45
	v_exp_f32_e32 v28, v28
	v_exp_f32_e32 v29, v29
	v_exp_f32_e64 v32, v32 clamp
	v_exp_f32_e64 v33, v33 clamp
	v_exp_f32_e32 v44, v46
	v_exp_f32_e32 v45, v47
	v_pk_fma_f32 v[58:59], v[80:81], s[2:3], 1.0 op_sel_hi:[1,0,0]
	v_pk_fma_f32 v[60:61], v[82:83], s[2:3], 1.0 op_sel_hi:[1,0,0]
	v_pk_fma_f32 v[52:53], v[52:53], s[2:3], 1.0 op_sel_hi:[1,0,0]
	v_pk_fma_f32 v[22:23], v[22:23], s[2:3], 1.0 op_sel_hi:[1,0,0]
	v_pk_fma_f32 v[54:55], v[54:55], s[2:3], 1.0 op_sel_hi:[1,0,0]
	v_pk_fma_f32 v[56:57], v[56:57], s[2:3], 1.0 op_sel_hi:[1,0,0]
	v_pk_fma_f32 v[30:31], v[30:31], s[2:3], 1.0 op_sel_hi:[1,0,0]
	v_pk_fma_f32 v[32:33], v[32:33], s[2:3], 1.0 op_sel_hi:[1,0,0]
	v_pk_fma_f32 v[46:47], v[78:79], v[58:59], v[58:59]
	v_pk_fma_f32 v[48:49], v[48:49], v[60:61], v[60:61]
	v_pk_fma_f32 v[50:51], v[50:51], v[52:53], v[52:53]
	v_pk_fma_f32 v[20:21], v[20:21], v[22:23], v[22:23]
	v_pk_fma_f32 v[24:25], v[24:25], v[54:55], v[54:55]
	v_pk_fma_f32 v[34:35], v[34:35], v[56:57], v[56:57]
	v_pk_fma_f32 v[26:27], v[26:27], v[30:31], v[30:31]
	v_pk_fma_f32 v[28:29], v[28:29], v[32:33], v[32:33]
	v_pk_fma_f32 v[58:59], v[58:59], s[6:7], v[40:41] op_sel_hi:[1,0,0] neg_lo:[1,0,0] neg_hi:[1,0,0]
	v_pk_fma_f32 v[60:61], v[60:61], s[6:7], v[40:41] op_sel_hi:[1,0,0] neg_lo:[1,0,0] neg_hi:[1,0,0]
	v_pk_fma_f32 v[52:53], v[52:53], s[6:7], v[40:41] op_sel_hi:[1,0,0] neg_lo:[1,0,0] neg_hi:[1,0,0]
	v_pk_fma_f32 v[22:23], v[22:23], s[6:7], v[40:41] op_sel_hi:[1,0,0] neg_lo:[1,0,0] neg_hi:[1,0,0]
	v_pk_fma_f32 v[54:55], v[54:55], s[6:7], v[40:41] op_sel_hi:[1,0,0] neg_lo:[1,0,0] neg_hi:[1,0,0]
	v_pk_fma_f32 v[56:57], v[56:57], s[6:7], v[40:41] op_sel_hi:[1,0,0] neg_lo:[1,0,0] neg_hi:[1,0,0]
	v_pk_fma_f32 v[30:31], v[30:31], s[6:7], v[40:41] op_sel_hi:[1,0,0] neg_lo:[1,0,0] neg_hi:[1,0,0]
	v_pk_fma_f32 v[32:33], v[32:33], s[6:7], v[40:41] op_sel_hi:[1,0,0] neg_lo:[1,0,0] neg_hi:[1,0,0]
	v_pk_fma_f32 v[46:47], v[4:5], v[46:47], v[46:47]
	v_pk_fma_f32 v[48:49], v[6:7], v[48:49], v[48:49]
	v_pk_fma_f32 v[50:51], v[8:9], v[50:51], v[50:51]
	v_pk_fma_f32 v[20:21], v[10:11], v[20:21], v[20:21]
	v_pk_fma_f32 v[24:25], v[12:13], v[24:25], v[24:25]
	v_pk_fma_f32 v[34:35], v[18:19], v[34:35], v[34:35]
	v_pk_fma_f32 v[26:27], v[36:37], v[26:27], v[26:27]
	v_pk_fma_f32 v[28:29], v[44:45], v[28:29], v[28:29]
	v_rcp_f32_e64 v46, v46 clamp
	v_rcp_f32_e64 v47, v47 clamp
	v_rcp_f32_e64 v48, v48 clamp
	v_rcp_f32_e64 v49, v49 clamp
	v_rcp_f32_e64 v50, v50 clamp
	v_rcp_f32_e64 v51, v51 clamp
	v_rcp_f32_e64 v20, v20 clamp
	v_rcp_f32_e64 v21, v21 clamp
	v_rcp_f32_e64 v24, v24 clamp
	v_rcp_f32_e64 v25, v25 clamp
	v_rcp_f32_e64 v34, v34 clamp
	v_rcp_f32_e64 v35, v35 clamp
	v_rcp_f32_e64 v26, v26 clamp
	v_rcp_f32_e64 v27, v27 clamp
	v_rcp_f32_e64 v28, v28 clamp
	v_rcp_f32_e64 v29, v29 clamp
	v_pk_mul_f32 v[46:47], v[58:59], v[46:47]
	v_pk_mul_f32 v[48:49], v[60:61], v[48:49]
	v_pk_mul_f32 v[50:51], v[52:53], v[50:51]
	v_pk_mul_f32 v[20:21], v[22:23], v[20:21]
	v_pk_mul_f32 v[22:23], v[54:55], v[24:25]
	v_pk_mul_f32 v[24:25], v[56:57], v[34:35]
	v_pk_mul_f32 v[26:27], v[30:31], v[26:27]
	v_pk_mul_f32 v[28:29], v[32:33], v[28:29]
	v_pk_fma_f32 v[4:5], v[4:5], v[46:47], v[46:47]
	v_pk_fma_f32 v[6:7], v[6:7], v[48:49], v[48:49]
	v_pk_fma_f32 v[8:9], v[8:9], v[50:51], v[50:51]
	v_pk_fma_f32 v[10:11], v[10:11], v[20:21], v[20:21]
	v_pk_fma_f32 v[12:13], v[12:13], v[22:23], v[22:23]
	v_pk_fma_f32 v[18:19], v[18:19], v[24:25], v[24:25]
	v_pk_fma_f32 v[30:31], v[36:37], v[26:27], v[26:27]
	v_pk_fma_f32 v[32:33], v[44:45], v[28:29], v[28:29]
	v_pk_fma_f32 v[4:5], v[4:5], v[4:5], s[4:5] neg_lo:[1,0,0] neg_hi:[1,0,0] clamp
	v_pk_fma_f32 v[6:7], v[6:7], v[6:7], s[4:5] neg_lo:[1,0,0] neg_hi:[1,0,0] clamp
	v_pk_fma_f32 v[8:9], v[8:9], v[8:9], s[4:5] neg_lo:[1,0,0] neg_hi:[1,0,0] clamp
	v_pk_fma_f32 v[10:11], v[10:11], v[10:11], s[4:5] neg_lo:[1,0,0] neg_hi:[1,0,0] clamp
	v_pk_fma_f32 v[12:13], v[12:13], v[12:13], s[4:5] neg_lo:[1,0,0] neg_hi:[1,0,0] clamp
	v_pk_fma_f32 v[18:19], v[18:19], v[18:19], s[4:5] neg_lo:[1,0,0] neg_hi:[1,0,0] clamp
	v_pk_fma_f32 v[30:31], v[30:31], v[30:31], s[4:5] neg_lo:[1,0,0] neg_hi:[1,0,0] clamp
	v_pk_fma_f32 v[32:33], v[32:33], v[32:33], s[4:5] neg_lo:[1,0,0] neg_hi:[1,0,0] clamp
	v_pk_fma_f32 v[8:9], v[8:9], v[8:9], s[8:9] op_sel_hi:[1,1,0]
	v_pk_fma_f32 v[10:11], v[10:11], v[10:11], s[8:9] op_sel_hi:[1,1,0]
	v_pk_fma_f32 v[12:13], v[12:13], v[12:13], s[8:9] op_sel_hi:[1,1,0]
	v_pk_fma_f32 v[18:19], v[18:19], v[18:19], s[8:9] op_sel_hi:[1,1,0]
	v_pk_fma_f32 v[32:33], v[32:33], v[32:33], s[8:9] op_sel_hi:[1,1,0]
	v_pk_fma_f32 v[4:5], v[4:5], v[4:5], s[8:9] op_sel_hi:[1,1,0]
	v_pk_fma_f32 v[6:7], v[6:7], v[6:7], s[8:9] op_sel_hi:[1,1,0]
	v_pk_fma_f32 v[30:31], v[30:31], v[30:31], s[8:9] op_sel_hi:[1,1,0]
	v_pk_mul_f32 v[8:9], v[50:51], v[8:9]
	v_pk_mul_f32 v[84:85], v[20:21], v[10:11]
	v_pk_mul_f32 v[86:87], v[22:23], v[12:13]
	v_pk_mul_f32 v[10:11], v[24:25], v[18:19]
	v_pk_mul_f32 v[12:13], v[28:29], v[32:33]
	v_pk_mul_f32 v[64:65], v[46:47], v[4:5]
	v_pk_mul_f32 v[82:83], v[48:49], v[6:7]
	v_pk_mul_f32 v[20:21], v[30:31], v[26:27]
	ds_read_b128 v[4:7], v72 offset:6144
	ds_read_b128 v[22:25], v71 offset:42368
	ds_read_b128 v[26:29], v72 offset:7168
	ds_read_b128 v[30:33], v71 offset:42432
	v_cvt_pk_f16_f32 v19, v84, v85
	v_cvt_pk_f16_f32 v18, v8, v9
	v_cvt_pk_f16_f32 v20, v20, v21
	s_waitcnt lgkmcnt(2)
	v_mfma_f32_16x16x32_f16 v[34:37], v[4:7], v[14:17], v[22:25]
	v_cvt_pk_f16_f32 v21, v12, v13
	v_mfma_f32_16x16x32_f16 v[44:47], v[4:7], v[0:3], v[22:25]
	ds_read_b128 v[4:7], v72 offset:8192
	ds_read_b128 v[48:51], v71 offset:42496
	s_waitcnt lgkmcnt(2)
	v_cvt_pk_f16_f32 v22, v64, v65
	v_mfma_f32_16x16x32_f16 v[52:55], v[26:29], v[14:17], v[30:33]
	v_cvt_pk_f16_f32 v23, v82, v83
	v_cvt_pk_f16_f32 v24, v86, v87
	v_mfma_f32_16x16x32_f16 v[26:29], v[26:29], v[0:3], v[30:33]
	ds_read_b128 v[56:59], v71 offset:42560
	v_exp_f32_e32 v86, v34
	v_exp_f32_e32 v87, v35
	ds_read_b128 v[30:33], v72 offset:9216
	s_waitcnt lgkmcnt(2)
	v_mfma_f32_16x16x32_f16 v[60:63], v[4:7], v[14:17], v[48:51]
	v_exp_f32_e64 v88, v52 clamp
	v_exp_f32_e64 v89, v53 clamp
	v_exp_f32_e64 v90, v54 clamp
	v_mfma_f32_16x16x32_f16 v[48:51], v[4:7], v[0:3], v[48:51]
	ds_read_b128 v[64:67], v72 offset:10240
	ds_read_b128 v[74:77], v71 offset:42624
	v_exp_f32_e32 v44, v44
	v_exp_f32_e32 v45, v45
	v_exp_f32_e32 v4, v60
	s_waitcnt lgkmcnt(2)
	v_mfma_f32_16x16x32_f16 v[78:81], v[30:33], v[14:17], v[56:59]
	v_exp_f32_e32 v5, v61
	v_exp_f32_e32 v60, v36
	v_exp_f32_e32 v61, v37
	v_mfma_f32_16x16x32_f16 v[30:33], v[30:33], v[0:3], v[56:59]
	ds_read_b128 v[82:85], v71 offset:42688
	v_exp_f32_e64 v91, v55 clamp
	v_exp_f32_e32 v6, v62
	ds_read_b128 v[56:59], v72 offset:11264
	s_waitcnt lgkmcnt(2)
	v_mfma_f32_16x16x32_f16 v[34:37], v[64:67], v[14:17], v[74:77]
	v_exp_f32_e32 v7, v63
	v_exp_f32_e32 v8, v48
	v_exp_f32_e32 v9, v49
	v_mfma_f32_16x16x32_f16 v[52:55], v[64:67], v[0:3], v[74:77]
	v_exp_f32_e64 v26, v26 clamp
	s_waitcnt lgkmcnt(0)
	v_mfma_f32_16x16x32_f16 v[14:17], v[56:59], v[14:17], v[82:85]
	v_exp_f32_e64 v27, v27 clamp
	v_exp_f32_e32 v46, v46
	v_exp_f32_e32 v47, v47
	v_mfma_f32_16x16x32_f16 v[56:59], v[56:59], v[0:3], v[82:85]
	v_exp_f32_e64 v28, v28 clamp
	v_exp_f32_e64 v29, v29 clamp
	v_exp_f32_e32 v0, v50
	v_exp_f32_e32 v1, v51
	v_exp_f32_e32 v2, v14
	v_exp_f32_e32 v3, v15
	v_exp_f32_e32 v14, v16
	v_exp_f32_e32 v15, v17
	v_exp_f32_e32 v16, v30
	v_exp_f32_e32 v17, v31
	v_exp_f32_e32 v48, v78
	v_exp_f32_e32 v49, v79
	v_exp_f32_e64 v34, v34 clamp
	v_exp_f32_e64 v35, v35 clamp
	v_exp_f32_e32 v50, v80
	v_exp_f32_e32 v51, v81
	v_exp_f32_e64 v36, v36 clamp
	v_exp_f32_e64 v37, v37 clamp
	v_exp_f32_e64 v30, v52 clamp
	v_exp_f32_e64 v31, v53 clamp
	v_exp_f32_e32 v52, v56
	v_exp_f32_e32 v53, v57
	v_exp_f32_e32 v32, v32
	v_exp_f32_e32 v33, v33
	v_exp_f32_e64 v54, v54 clamp
	v_exp_f32_e64 v55, v55 clamp
	v_exp_f32_e32 v56, v58
	v_cvt_pk_f16_f32 v25, v10, v11
	v_exp_f32_e32 v57, v59
	v_pk_fma_f32 v[30:31], v[30:31], s[2:3], 1.0 op_sel_hi:[1,0,0]
	v_pk_fma_f32 v[10:11], v[88:89], s[2:3], 1.0 op_sel_hi:[1,0,0]
	v_pk_fma_f32 v[12:13], v[90:91], s[2:3], 1.0 op_sel_hi:[1,0,0]
	v_pk_fma_f32 v[26:27], v[26:27], s[2:3], 1.0 op_sel_hi:[1,0,0]
	v_pk_fma_f32 v[28:29], v[28:29], s[2:3], 1.0 op_sel_hi:[1,0,0]
	v_pk_fma_f32 v[34:35], v[34:35], s[2:3], 1.0 op_sel_hi:[1,0,0]
	v_pk_fma_f32 v[36:37], v[36:37], s[2:3], 1.0 op_sel_hi:[1,0,0]
	v_pk_fma_f32 v[54:55], v[54:55], s[2:3], 1.0 op_sel_hi:[1,0,0]
	v_pk_fma_f32 v[16:17], v[16:17], v[30:31], v[30:31]
	v_pk_fma_f32 v[58:59], v[86:87], v[10:11], v[10:11]
	v_pk_fma_f32 v[10:11], v[10:11], s[6:7], v[40:41] op_sel_hi:[1,0,0] neg_lo:[1,0,0] neg_hi:[1,0,0]
	v_pk_fma_f32 v[60:61], v[60:61], v[12:13], v[12:13]
	v_pk_fma_f32 v[12:13], v[12:13], s[6:7], v[40:41] op_sel_hi:[1,0,0] neg_lo:[1,0,0] neg_hi:[1,0,0]
	v_pk_fma_f32 v[44:45], v[44:45], v[26:27], v[26:27]
	v_pk_fma_f32 v[46:47], v[46:47], v[28:29], v[28:29]
	v_pk_fma_f32 v[48:49], v[48:49], v[34:35], v[34:35]
	v_pk_fma_f32 v[50:51], v[50:51], v[36:37], v[36:37]
	v_pk_fma_f32 v[32:33], v[32:33], v[54:55], v[54:55]
	v_pk_fma_f32 v[16:17], v[52:53], v[16:17], v[16:17]
	v_pk_fma_f32 v[26:27], v[26:27], s[6:7], v[40:41] op_sel_hi:[1,0,0] neg_lo:[1,0,0] neg_hi:[1,0,0]
	v_pk_fma_f32 v[28:29], v[28:29], s[6:7], v[40:41] op_sel_hi:[1,0,0] neg_lo:[1,0,0] neg_hi:[1,0,0]
	v_pk_fma_f32 v[34:35], v[34:35], s[6:7], v[40:41] op_sel_hi:[1,0,0] neg_lo:[1,0,0] neg_hi:[1,0,0]
	v_pk_fma_f32 v[36:37], v[36:37], s[6:7], v[40:41] op_sel_hi:[1,0,0] neg_lo:[1,0,0] neg_hi:[1,0,0]
	v_pk_fma_f32 v[30:31], v[30:31], s[6:7], v[40:41] op_sel_hi:[1,0,0] neg_lo:[1,0,0] neg_hi:[1,0,0]
	v_pk_fma_f32 v[54:55], v[54:55], s[6:7], v[40:41] op_sel_hi:[1,0,0] neg_lo:[1,0,0] neg_hi:[1,0,0]
	v_pk_fma_f32 v[58:59], v[4:5], v[58:59], v[58:59]
	v_pk_fma_f32 v[60:61], v[6:7], v[60:61], v[60:61]
	v_pk_fma_f32 v[44:45], v[8:9], v[44:45], v[44:45]
	v_pk_fma_f32 v[46:47], v[0:1], v[46:47], v[46:47]
	v_pk_fma_f32 v[48:49], v[2:3], v[48:49], v[48:49]
	v_pk_fma_f32 v[50:51], v[14:15], v[50:51], v[50:51]
	v_pk_fma_f32 v[32:33], v[56:57], v[32:33], v[32:33]
	v_rcp_f32_e64 v16, v16 clamp
	v_rcp_f32_e64 v17, v17 clamp
	v_rcp_f32_e64 v58, v58 clamp
	v_rcp_f32_e64 v59, v59 clamp
	v_rcp_f32_e64 v60, v60 clamp
	v_rcp_f32_e64 v61, v61 clamp
	v_rcp_f32_e64 v44, v44 clamp
	v_rcp_f32_e64 v45, v45 clamp
	v_rcp_f32_e64 v46, v46 clamp
	v_rcp_f32_e64 v47, v47 clamp
	v_rcp_f32_e64 v48, v48 clamp
	v_rcp_f32_e64 v49, v49 clamp
	v_rcp_f32_e64 v50, v50 clamp
	v_rcp_f32_e64 v51, v51 clamp
	v_rcp_f32_e64 v32, v32 clamp
	v_rcp_f32_e64 v33, v33 clamp
	v_pk_mul_f32 v[10:11], v[10:11], v[58:59]
	v_pk_mul_f32 v[12:13], v[12:13], v[60:61]
	v_pk_mul_f32 v[26:27], v[26:27], v[44:45]
	v_pk_mul_f32 v[34:35], v[34:35], v[48:49]
	v_pk_mul_f32 v[36:37], v[36:37], v[50:51]
	v_pk_mul_f32 v[28:29], v[28:29], v[46:47]
	v_pk_mul_f32 v[16:17], v[30:31], v[16:17]
	v_pk_mul_f32 v[30:31], v[54:55], v[32:33]
	v_pk_fma_f32 v[4:5], v[4:5], v[10:11], v[10:11]
	v_pk_fma_f32 v[6:7], v[6:7], v[12:13], v[12:13]
	v_pk_fma_f32 v[8:9], v[8:9], v[26:27], v[26:27]
	v_pk_fma_f32 v[2:3], v[2:3], v[34:35], v[34:35]
	v_pk_fma_f32 v[14:15], v[14:15], v[36:37], v[36:37]
	v_pk_fma_f32 v[0:1], v[0:1], v[28:29], v[28:29]
	v_pk_fma_f32 v[32:33], v[52:53], v[16:17], v[16:17]
	v_pk_fma_f32 v[44:45], v[56:57], v[30:31], v[30:31]
	v_pk_fma_f32 v[4:5], v[4:5], v[4:5], s[4:5] neg_lo:[1,0,0] neg_hi:[1,0,0] clamp
	v_pk_fma_f32 v[6:7], v[6:7], v[6:7], s[4:5] neg_lo:[1,0,0] neg_hi:[1,0,0] clamp
	v_pk_fma_f32 v[8:9], v[8:9], v[8:9], s[4:5] neg_lo:[1,0,0] neg_hi:[1,0,0] clamp
	v_pk_fma_f32 v[0:1], v[0:1], v[0:1], s[4:5] neg_lo:[1,0,0] neg_hi:[1,0,0] clamp
	v_pk_fma_f32 v[2:3], v[2:3], v[2:3], s[4:5] neg_lo:[1,0,0] neg_hi:[1,0,0] clamp
	v_pk_fma_f32 v[14:15], v[14:15], v[14:15], s[4:5] neg_lo:[1,0,0] neg_hi:[1,0,0] clamp
	v_pk_fma_f32 v[32:33], v[32:33], v[32:33], s[4:5] neg_lo:[1,0,0] neg_hi:[1,0,0] clamp
	v_pk_fma_f32 v[44:45], v[44:45], v[44:45], s[4:5] neg_lo:[1,0,0] neg_hi:[1,0,0] clamp
	v_pk_fma_f32 v[32:33], v[32:33], v[32:33], s[8:9] op_sel_hi:[1,1,0]
	v_pk_fma_f32 v[4:5], v[4:5], v[4:5], s[8:9] op_sel_hi:[1,1,0]
	v_pk_fma_f32 v[6:7], v[6:7], v[6:7], s[8:9] op_sel_hi:[1,1,0]
	v_pk_fma_f32 v[8:9], v[8:9], v[8:9], s[8:9] op_sel_hi:[1,1,0]
	v_pk_fma_f32 v[0:1], v[0:1], v[0:1], s[8:9] op_sel_hi:[1,1,0]
	v_pk_fma_f32 v[2:3], v[2:3], v[2:3], s[8:9] op_sel_hi:[1,1,0]
	v_pk_fma_f32 v[14:15], v[14:15], v[14:15], s[8:9] op_sel_hi:[1,1,0]
	v_pk_fma_f32 v[44:45], v[44:45], v[44:45], s[8:9] op_sel_hi:[1,1,0]
	v_pk_mul_f32 v[16:17], v[32:33], v[16:17]
	v_pk_mul_f32 v[52:53], v[10:11], v[4:5]
	v_pk_mul_f32 v[54:55], v[12:13], v[6:7]
	v_pk_mul_f32 v[26:27], v[26:27], v[8:9]
	v_pk_mul_f32 v[28:29], v[28:29], v[0:1]
	v_pk_mul_f32 v[56:57], v[34:35], v[2:3]
	v_pk_mul_f32 v[58:59], v[36:37], v[14:15]
	v_pk_mul_f32 v[60:61], v[30:31], v[44:45]
	s_cmp_lt_u32 s33, 8
	s_cbranch_scc1 .Lprio_half
	s_setprio 0
.Lprio_half:
	ds_read_b128 v[0:3], v72 offset:12288
	ds_read_b128 v[4:7], v71 offset:42752
	ds_read_b128 v[8:11], v72 offset:13312
	ds_read_b128 v[12:15], v72 offset:14336
	ds_read_b128 v[34:37], v72 offset:15360
	ds_read_b128 v[44:47], v71 offset:42816
	v_cvt_pk_f16_f32 v30, v52, v53
	v_cvt_pk_f16_f32 v26, v26, v27
	v_cvt_pk_f16_f32 v31, v54, v55
	s_waitcnt lgkmcnt(4)
	v_mfma_f32_16x16x32_f16 v[48:51], v[0:3], v[22:25], v[4:7]
	v_cvt_pk_f16_f32 v32, v56, v57
	v_cvt_pk_f16_f32 v33, v58, v59
	v_cvt_pk_f16_f32 v27, v28, v29
	v_mfma_f32_16x16x32_f16 v[0:3], v[0:3], v[18:21], v[4:7]
	v_cvt_pk_f16_f32 v28, v16, v17
	s_add_i32 s11, s9, s12
	s_waitcnt lgkmcnt(3)
	v_mfma_f32_16x16x32_f16 v[48:51], v[8:11], v[30:33], v[48:51]
	s_cmp_lt_i32 s11, 0x8000
	v_cvt_pk_f16_f32 v29, v60, v61
	s_cselect_b32 s10, s11, s10
	s_ashr_i32 s11, s10, 31
	v_mfma_f32_16x16x32_f16 v[52:55], v[8:11], v[26:29], v[0:3]
	ds_read_b128 v[4:7], v72 offset:17408
	ds_read_b128 v[8:11], v71 offset:42880
	s_lshl_b64 s[10:11], s[10:11], 12
	s_add_u32 s10, s10, s36
	s_addc_u32 s11, s11, s37
	ds_read_b128 v[0:3], v72 offset:16384
	s_waitcnt lgkmcnt(3)
	v_exp_f32_e32 v106, v48
	v_mfma_f32_16x16x32_f16 v[56:59], v[12:15], v[22:25], v[44:47]
	v_exp_f32_e32 v107, v49
	v_exp_f32_e32 v110, v50
	v_mfma_f32_16x16x32_f16 v[12:15], v[12:15], v[18:21], v[44:47]
	v_exp_f32_e32 v111, v51
	v_exp_f32_e32 v114, v52
	v_mfma_f32_16x16x32_f16 v[44:47], v[34:37], v[30:33], v[56:59]
	v_exp_f32_e32 v115, v53
	v_mfma_f32_16x16x32_f16 v[56:59], v[34:37], v[26:29], v[12:15]
	ds_read_b128 v[34:37], v72 offset:19456
	ds_read_b128 v[60:63], v71 offset:42944
	s_nop 4
	v_exp_f32_e64 v108, v44 clamp
	ds_read_b128 v[12:15], v72 offset:18432
	s_waitcnt lgkmcnt(3)
	v_mfma_f32_16x16x32_f16 v[64:67], v[0:3], v[22:25], v[8:11]
	v_exp_f32_e64 v109, v45 clamp
	v_mfma_f32_16x16x32_f16 v[0:3], v[0:3], v[18:21], v[8:11]
	v_exp_f32_e64 v116, v56 clamp
	v_mfma_f32_16x16x32_f16 v[64:67], v[4:7], v[30:33], v[64:67]
	v_exp_f32_e64 v59, v59 clamp
	v_mfma_f32_16x16x32_f16 v[74:77], v[4:7], v[26:29], v[0:3]
	ds_read_b128 v[78:81], v72 offset:20480
	ds_read_b128 v[82:85], v72 offset:21504
	ds_read_b128 v[86:89], v71 offset:43008
	s_waitcnt lgkmcnt(3)
	v_exp_f32_e64 v58, v58 clamp
	v_mfma_f32_16x16x32_f16 v[6:9], v[12:15], v[22:25], v[60:63]
	v_exp_f32_e64 v117, v57 clamp
	v_mfma_f32_16x16x32_f16 v[60:63], v[12:15], v[18:21], v[60:63]
	global_load_dwordx4 v[10:13], v39, s[10:11] offset:16
	global_load_dwordx4 v[14:17], v39, s[10:11]
	global_load_dwordx4 v[2:5], v39, s[10:11] offset:2064
	v_exp_f32_e64 v113, v47 clamp
	v_mfma_f32_16x16x32_f16 v[90:93], v[34:37], v[30:33], v[6:9]
	v_exp_f32_e64 v112, v46 clamp
	v_mfma_f32_16x16x32_f16 v[60:63], v[34:37], v[26:29], v[60:63]
	s_nop 1
	global_load_dwordx4 v[6:9], v39, s[10:11] offset:2048
	ds_read_b128 v[94:97], v72 offset:22528
	ds_read_b128 v[98:101], v72 offset:23552
	ds_read_b128 v[102:105], v71 offset:43072
	s_waitcnt lgkmcnt(3)
	v_exp_f32_e32 v0, v64
	v_mfma_f32_16x16x32_f16 v[44:47], v[78:81], v[22:25], v[86:89]
	v_exp_f32_e32 v1, v65
	v_exp_f32_e32 v34, v66
	v_mfma_f32_16x16x32_f16 v[48:51], v[78:81], v[18:21], v[86:89]
	v_exp_f32_e32 v35, v67
	v_exp_f32_e32 v36, v74
	v_exp_f32_e32 v37, v75
	v_mfma_f32_16x16x32_f16 v[64:67], v[82:85], v[30:33], v[44:47]
	v_exp_f32_e32 v74, v54
	v_exp_f32_e32 v75, v55
	v_exp_f32_e32 v78, v92
	v_mfma_f32_16x16x32_f16 v[50:53], v[82:85], v[26:29], v[48:51]
	v_exp_f32_e32 v44, v76
	v_exp_f32_e32 v45, v77
	v_exp_f32_e32 v76, v90
	s_waitcnt lgkmcnt(0)
	v_mfma_f32_16x16x32_f16 v[46:49], v[94:97], v[22:25], v[102:105]
	v_exp_f32_e32 v77, v91
	v_exp_f32_e64 v64, v64 clamp
	v_exp_f32_e64 v65, v65 clamp
	v_mfma_f32_16x16x32_f16 v[54:57], v[94:97], v[18:21], v[102:105]
	v_exp_f32_e32 v79, v93
	v_exp_f32_e64 v66, v66 clamp
	v_exp_f32_e64 v67, v67 clamp
	v_mfma_f32_16x16x32_f16 v[46:49], v[98:101], v[30:33], v[46:49]
	v_exp_f32_e32 v60, v60
	v_exp_f32_e32 v61, v61
	v_exp_f32_e64 v50, v50 clamp
	v_mfma_f32_16x16x32_f16 v[54:57], v[98:101], v[26:29], v[54:57]
	v_exp_f32_e64 v51, v51 clamp
	v_exp_f32_e32 v62, v62
	v_exp_f32_e32 v63, v63
	v_exp_f32_e64 v52, v52 clamp
	v_exp_f32_e32 v46, v46
	v_exp_f32_e32 v47, v47
	v_exp_f32_e32 v48, v48
	v_exp_f32_e32 v49, v49
	v_exp_f32_e32 v54, v54
	v_exp_f32_e32 v55, v55
	v_exp_f32_e64 v53, v53 clamp
	v_exp_f32_e32 v56, v56
	v_exp_f32_e32 v57, v57
	v_pk_fma_f32 v[80:81], v[108:109], s[2:3], 1.0 op_sel_hi:[1,0,0]
	v_pk_fma_f32 v[82:83], v[112:113], s[2:3], 1.0 op_sel_hi:[1,0,0]
	v_pk_fma_f32 v[84:85], v[116:117], s[2:3], 1.0 op_sel_hi:[1,0,0]
	v_pk_fma_f32 v[58:59], v[58:59], s[2:3], 1.0 op_sel_hi:[1,0,0]
	v_pk_fma_f32 v[64:65], v[64:65], s[2:3], 1.0 op_sel_hi:[1,0,0]
	v_pk_fma_f32 v[66:67], v[66:67], s[2:3], 1.0 op_sel_hi:[1,0,0]
	v_pk_fma_f32 v[50:51], v[50:51], s[2:3], 1.0 op_sel_hi:[1,0,0]
	v_pk_fma_f32 v[52:53], v[52:53], s[2:3], 1.0 op_sel_hi:[1,0,0]
	v_pk_fma_f32 v[86:87], v[106:107], v[80:81], v[80:81]
	v_pk_fma_f32 v[88:89], v[110:111], v[82:83], v[82:83]
	v_pk_fma_f32 v[90:91], v[114:115], v[84:85], v[84:85]
	v_pk_fma_f32 v[74:75], v[74:75], v[58:59], v[58:59]
	v_pk_fma_f32 v[76:77], v[76:77], v[64:65], v[64:65]
	v_pk_fma_f32 v[78:79], v[78:79], v[66:67], v[66:67]
	v_pk_fma_f32 v[60:61], v[60:61], v[50:51], v[50:51]
	v_pk_fma_f32 v[62:63], v[62:63], v[52:53], v[52:53]
	v_pk_fma_f32 v[80:81], v[80:81], s[6:7], v[40:41] op_sel_hi:[1,0,0] neg_lo:[1,0,0] neg_hi:[1,0,0]
	v_pk_fma_f32 v[82:83], v[82:83], s[6:7], v[40:41] op_sel_hi:[1,0,0] neg_lo:[1,0,0] neg_hi:[1,0,0]
	v_pk_fma_f32 v[84:85], v[84:85], s[6:7], v[40:41] op_sel_hi:[1,0,0] neg_lo:[1,0,0] neg_hi:[1,0,0]
	v_pk_fma_f32 v[58:59], v[58:59], s[6:7], v[40:41] op_sel_hi:[1,0,0] neg_lo:[1,0,0] neg_hi:[1,0,0]
	v_pk_fma_f32 v[64:65], v[64:65], s[6:7], v[40:41] op_sel_hi:[1,0,0] neg_lo:[1,0,0] neg_hi:[1,0,0]
	v_pk_fma_f32 v[66:67], v[66:67], s[6:7], v[40:41] op_sel_hi:[1,0,0] neg_lo:[1,0,0] neg_hi:[1,0,0]
	v_pk_fma_f32 v[50:51], v[50:51], s[6:7], v[40:41] op_sel_hi:[1,0,0] neg_lo:[1,0,0] neg_hi:[1,0,0]
	v_pk_fma_f32 v[52:53], v[52:53], s[6:7], v[40:41] op_sel_hi:[1,0,0] neg_lo:[1,0,0] neg_hi:[1,0,0]
	v_pk_fma_f32 v[86:87], v[0:1], v[86:87], v[86:87]
	v_pk_fma_f32 v[88:89], v[34:35], v[88:89], v[88:89]
	v_pk_fma_f32 v[90:91], v[36:37], v[90:91], v[90:91]
	v_pk_fma_f32 v[74:75], v[44:45], v[74:75], v[74:75]
	v_pk_fma_f32 v[76:77], v[46:47], v[76:77], v[76:77]
	v_pk_fma_f32 v[78:79], v[48:49], v[78:79], v[78:79]
	v_pk_fma_f32 v[60:61], v[54:55], v[60:61], v[60:61]
	v_pk_fma_f32 v[62:63], v[56:57], v[62:63], v[62:63]
	v_rcp_f32_e64 v86, v86 clamp
	v_rcp_f32_e64 v87, v87 clamp
	v_rcp_f32_e64 v88, v88 clamp
	v_rcp_f32_e64 v89, v89 clamp
	v_rcp_f32_e64 v90, v90 clamp
	v_rcp_f32_e64 v91, v91 clamp
	v_rcp_f32_e64 v74, v74 clamp
	v_rcp_f32_e64 v75, v75 clamp
	v_rcp_f32_e64 v76, v76 clamp
	v_rcp_f32_e64 v77, v77 clamp
	v_rcp_f32_e64 v78, v78 clamp
	v_rcp_f32_e64 v79, v79 clamp
	v_rcp_f32_e64 v60, v60 clamp
	v_rcp_f32_e64 v61, v61 clamp
	v_rcp_f32_e64 v62, v62 clamp
	v_rcp_f32_e64 v63, v63 clamp
	v_pk_mul_f32 v[80:81], v[80:81], v[86:87]
	v_pk_mul_f32 v[82:83], v[82:83], v[88:89]
	v_pk_mul_f32 v[84:85], v[84:85], v[90:91]
	v_pk_mul_f32 v[58:59], v[58:59], v[74:75]
	v_pk_mul_f32 v[64:65], v[64:65], v[76:77]
	v_pk_mul_f32 v[66:67], v[66:67], v[78:79]
	v_pk_mul_f32 v[50:51], v[50:51], v[60:61]
	v_pk_mul_f32 v[60:61], v[52:53], v[62:63]
	v_pk_fma_f32 v[0:1], v[0:1], v[80:81], v[80:81]
	v_pk_fma_f32 v[34:35], v[34:35], v[82:83], v[82:83]
	v_pk_fma_f32 v[36:37], v[36:37], v[84:85], v[84:85]
	v_pk_fma_f32 v[44:45], v[44:45], v[58:59], v[58:59]
	v_pk_fma_f32 v[46:47], v[46:47], v[64:65], v[64:65]
	v_pk_fma_f32 v[48:49], v[48:49], v[66:67], v[66:67]
	v_pk_fma_f32 v[52:53], v[54:55], v[50:51], v[50:51]
	v_pk_fma_f32 v[54:55], v[56:57], v[60:61], v[60:61]
	v_pk_fma_f32 v[0:1], v[0:1], v[0:1], s[4:5] neg_lo:[1,0,0] neg_hi:[1,0,0] clamp
	v_pk_fma_f32 v[34:35], v[34:35], v[34:35], s[4:5] neg_lo:[1,0,0] neg_hi:[1,0,0] clamp
	v_pk_fma_f32 v[36:37], v[36:37], v[36:37], s[4:5] neg_lo:[1,0,0] neg_hi:[1,0,0] clamp
	v_pk_fma_f32 v[44:45], v[44:45], v[44:45], s[4:5] neg_lo:[1,0,0] neg_hi:[1,0,0] clamp
	v_pk_fma_f32 v[46:47], v[46:47], v[46:47], s[4:5] neg_lo:[1,0,0] neg_hi:[1,0,0] clamp
	v_pk_fma_f32 v[48:49], v[48:49], v[48:49], s[4:5] neg_lo:[1,0,0] neg_hi:[1,0,0] clamp
	v_pk_fma_f32 v[52:53], v[52:53], v[52:53], s[4:5] neg_lo:[1,0,0] neg_hi:[1,0,0] clamp
	v_pk_fma_f32 v[54:55], v[54:55], v[54:55], s[4:5] neg_lo:[1,0,0] neg_hi:[1,0,0] clamp
	v_pk_fma_f32 v[0:1], v[0:1], v[0:1], s[8:9] op_sel_hi:[1,1,0]
	v_pk_fma_f32 v[56:57], v[34:35], v[34:35], s[8:9] op_sel_hi:[1,1,0]
	v_pk_fma_f32 v[36:37], v[36:37], v[36:37], s[8:9] op_sel_hi:[1,1,0]
	v_pk_fma_f32 v[44:45], v[44:45], v[44:45], s[8:9] op_sel_hi:[1,1,0]
	v_pk_fma_f32 v[46:47], v[46:47], v[46:47], s[8:9] op_sel_hi:[1,1,0]
	v_pk_fma_f32 v[48:49], v[48:49], v[48:49], s[8:9] op_sel_hi:[1,1,0]
	v_pk_fma_f32 v[62:63], v[52:53], v[52:53], s[8:9] op_sel_hi:[1,1,0]
	v_pk_fma_f32 v[74:75], v[54:55], v[54:55], s[8:9] op_sel_hi:[1,1,0]
	v_pk_mul_f32 v[34:35], v[80:81], v[0:1]
	v_pk_mul_f32 v[56:57], v[82:83], v[56:57]
	v_pk_mul_f32 v[36:37], v[84:85], v[36:37]
	v_pk_mul_f32 v[52:53], v[58:59], v[44:45]
	v_pk_mul_f32 v[54:55], v[64:65], v[46:47]
	v_pk_mul_f32 v[0:1], v[66:67], v[48:49]
	v_pk_mul_f32 v[46:47], v[62:63], v[50:51]
	v_pk_mul_f32 v[44:45], v[60:61], v[74:75]
	ds_read_b128 v[48:51], v72 offset:24576
	ds_read_b128 v[58:61], v71 offset:43136
	ds_read_b128 v[62:65], v72 offset:25600
	ds_read_b128 v[74:77], v72 offset:26624
	ds_read_b128 v[78:81], v72 offset:27648
	ds_read_b128 v[82:85], v71 offset:43200
	v_cvt_pk_f16_f32 v34, v34, v35
	s_waitcnt lgkmcnt(4)
	v_mfma_f32_16x16x32_f16 v[86:89], v[48:51], v[22:25], v[58:61]
	v_cvt_pk_f16_f32 v35, v56, v57
	v_mfma_f32_16x16x32_f16 v[48:51], v[48:51], v[18:21], v[58:61]
	s_waitcnt lgkmcnt(3)
	v_mfma_f32_16x16x32_f16 v[58:61], v[62:65], v[30:33], v[86:89]
	v_mfma_f32_16x16x32_f16 v[86:89], v[62:65], v[26:29], v[48:51]
	ds_read_b128 v[62:65], v72 offset:29696
	ds_read_b128 v[90:93], v71 offset:43264
	s_nop 2
	ds_read_b128 v[48:51], v72 offset:28672
	s_waitcnt lgkmcnt(3)
	v_mfma_f32_16x16x32_f16 v[94:97], v[74:77], v[22:25], v[82:85]
	v_exp_f32_e32 v120, v86
	v_mfma_f32_16x16x32_f16 v[74:77], v[74:77], v[18:21], v[82:85]
	v_exp_f32_e32 v123, v89
	v_mfma_f32_16x16x32_f16 v[82:85], v[78:81], v[30:33], v[94:97]
	v_exp_f32_e32 v122, v88
	v_mfma_f32_16x16x32_f16 v[74:77], v[78:81], v[26:29], v[74:77]
	ds_read_b128 v[78:81], v72 offset:30720
	s_nop 0
	ds_read_b128 v[94:97], v72 offset:31744
	ds_read_b128 v[98:101], v71 offset:43328
	s_waitcnt lgkmcnt(3)
	v_exp_f32_e32 v121, v87
	v_mfma_f32_16x16x32_f16 v[102:105], v[48:51], v[22:25], v[90:93]
	v_exp_f32_e64 v66, v82 clamp
	v_exp_f32_e64 v67, v83 clamp
	v_exp_f32_e64 v118, v84 clamp
	v_mfma_f32_16x16x32_f16 v[48:51], v[48:51], v[18:21], v[90:93]
	v_exp_f32_e64 v119, v85 clamp
	v_exp_f32_e64 v124, v74 clamp
	v_exp_f32_e64 v125, v75 clamp
	v_mfma_f32_16x16x32_f16 v[90:93], v[62:65], v[30:33], v[102:105]
	v_exp_f32_e64 v126, v76 clamp
	v_exp_f32_e64 v127, v77 clamp
	v_mfma_f32_16x16x32_f16 v[102:105], v[62:65], v[26:29], v[48:51]
	ds_read_b128 v[106:109], v72 offset:32768
	ds_read_b128 v[110:113], v72 offset:33792
	v_exp_f32_e32 v62, v58
	v_exp_f32_e32 v63, v59
	v_exp_f32_e32 v64, v60
	v_exp_f32_e32 v65, v61
	ds_read_b128 v[114:117], v71 offset:43392
	s_waitcnt lgkmcnt(3)
	v_mfma_f32_16x16x32_f16 v[58:61], v[78:81], v[22:25], v[98:101]
	v_exp_f32_e32 v48, v90
	v_exp_f32_e32 v49, v91
	v_mfma_f32_16x16x32_f16 v[78:81], v[78:81], v[18:21], v[98:101]
	v_exp_f32_e32 v51, v93
	v_mfma_f32_16x16x32_f16 v[82:85], v[94:97], v[30:33], v[58:61]
	v_exp_f32_e32 v50, v92
	v_mfma_f32_16x16x32_f16 v[78:81], v[94:97], v[26:29], v[78:81]
	ds_read_b128 v[86:89], v72 offset:34816
	ds_read_b128 v[90:93], v72 offset:35840
	ds_read_b128 v[94:97], v71 offset:43456
	s_waitcnt lgkmcnt(3)
	v_exp_f32_e32 v58, v102
	v_mfma_f32_16x16x32_f16 v[74:77], v[106:109], v[22:25], v[114:117]
	v_exp_f32_e32 v59, v103
	v_exp_f32_e32 v60, v104
	v_mfma_f32_16x16x32_f16 v[98:101], v[106:109], v[18:21], v[114:117]
	v_exp_f32_e32 v61, v105
	v_exp_f32_e32 v102, v82
	v_exp_f32_e32 v103, v83
	v_exp_f32_e32 v104, v84
	v_mfma_f32_16x16x32_f16 v[74:77], v[110:113], v[30:33], v[74:77]
	v_exp_f32_e32 v105, v85
	v_mfma_f32_16x16x32_f16 v[82:85], v[110:113], v[26:29], v[98:101]
	s_waitcnt lgkmcnt(0)
	v_mfma_f32_16x16x32_f16 v[18:21], v[86:89], v[18:21], v[94:97]
	s_nop 4
	v_exp_f32_e64 v106, v74 clamp
	v_exp_f32_e64 v107, v75 clamp
	v_exp_f32_e64 v108, v76 clamp
	v_exp_f32_e64 v109, v77 clamp
	v_mfma_f32_16x16x32_f16 v[74:77], v[86:89], v[22:25], v[94:97]
	v_cvt_pk_f16_f32 v22, v36, v37
	v_cvt_pk_f16_f32 v23, v52, v53
	v_cvt_pk_f16_f32 v36, v54, v55
	v_mfma_f32_16x16x32_f16 v[18:21], v[90:93], v[26:29], v[18:21]
	v_exp_f32_e32 v52, v78
	v_exp_f32_e32 v53, v79
	v_exp_f32_e64 v54, v82 clamp
	v_mfma_f32_16x16x32_f16 v[30:33], v[90:93], v[30:33], v[74:77]
	v_exp_f32_e64 v55, v83 clamp
	v_exp_f32_e64 v28, v84 clamp
	v_exp_f32_e64 v29, v85 clamp
	v_cvt_pk_f16_f32 v24, v46, v47
	v_exp_f32_e32 v18, v18
	v_exp_f32_e32 v19, v19
	v_exp_f32_e32 v26, v80
	v_exp_f32_e32 v27, v81
	v_exp_f32_e32 v30, v30
	v_exp_f32_e32 v31, v31
	v_exp_f32_e32 v32, v32
	v_exp_f32_e32 v33, v33
	v_exp_f32_e32 v20, v20
	v_cvt_pk_f16_f32 v37, v0, v1
	v_cvt_pk_f16_f32 v25, v44, v45
	v_exp_f32_e32 v21, v21
	v_pk_fma_f32 v[0:1], v[66:67], s[2:3], 1.0 op_sel_hi:[1,0,0]
	v_pk_fma_f32 v[44:45], v[118:119], s[2:3], 1.0 op_sel_hi:[1,0,0]
	v_pk_fma_f32 v[46:47], v[124:125], s[2:3], 1.0 op_sel_hi:[1,0,0]
	v_pk_fma_f32 v[56:57], v[126:127], s[2:3], 1.0 op_sel_hi:[1,0,0]
	v_pk_fma_f32 v[66:67], v[106:107], s[2:3], 1.0 op_sel_hi:[1,0,0]
	v_pk_fma_f32 v[74:75], v[108:109], s[2:3], 1.0 op_sel_hi:[1,0,0]
	v_pk_fma_f32 v[54:55], v[54:55], s[2:3], 1.0 op_sel_hi:[1,0,0]
	v_pk_fma_f32 v[28:29], v[28:29], s[2:3], 1.0 op_sel_hi:[1,0,0]
	v_pk_fma_f32 v[62:63], v[62:63], v[0:1], v[0:1]
	v_pk_fma_f32 v[64:65], v[64:65], v[44:45], v[44:45]
	v_pk_fma_f32 v[76:77], v[120:121], v[46:47], v[46:47]
	v_pk_fma_f32 v[78:79], v[122:123], v[56:57], v[56:57]
	v_pk_fma_f32 v[80:81], v[102:103], v[66:67], v[66:67]
	v_pk_fma_f32 v[82:83], v[104:105], v[74:75], v[74:75]
	v_pk_fma_f32 v[52:53], v[52:53], v[54:55], v[54:55]
	v_pk_fma_f32 v[26:27], v[26:27], v[28:29], v[28:29]
	v_pk_fma_f32 v[0:1], v[0:1], s[6:7], v[40:41] op_sel_hi:[1,0,0] neg_lo:[1,0,0] neg_hi:[1,0,0]
	v_pk_fma_f32 v[44:45], v[44:45], s[6:7], v[40:41] op_sel_hi:[1,0,0] neg_lo:[1,0,0] neg_hi:[1,0,0]
	v_pk_fma_f32 v[46:47], v[46:47], s[6:7], v[40:41] op_sel_hi:[1,0,0] neg_lo:[1,0,0] neg_hi:[1,0,0]
	v_pk_fma_f32 v[56:57], v[56:57], s[6:7], v[40:41] op_sel_hi:[1,0,0] neg_lo:[1,0,0] neg_hi:[1,0,0]
	v_pk_fma_f32 v[66:67], v[66:67], s[6:7], v[40:41] op_sel_hi:[1,0,0] neg_lo:[1,0,0] neg_hi:[1,0,0]
	v_pk_fma_f32 v[74:75], v[74:75], s[6:7], v[40:41] op_sel_hi:[1,0,0] neg_lo:[1,0,0] neg_hi:[1,0,0]
	v_pk_fma_f32 v[54:55], v[54:55], s[6:7], v[40:41] op_sel_hi:[1,0,0] neg_lo:[1,0,0] neg_hi:[1,0,0]
	v_pk_fma_f32 v[28:29], v[28:29], s[6:7], v[40:41] op_sel_hi:[1,0,0] neg_lo:[1,0,0] neg_hi:[1,0,0]
	v_pk_fma_f32 v[62:63], v[48:49], v[62:63], v[62:63]
	v_pk_fma_f32 v[64:65], v[50:51], v[64:65], v[64:65]
	v_pk_fma_f32 v[76:77], v[58:59], v[76:77], v[76:77]
	v_pk_fma_f32 v[78:79], v[60:61], v[78:79], v[78:79]
	v_pk_fma_f32 v[80:81], v[30:31], v[80:81], v[80:81]
	v_pk_fma_f32 v[82:83], v[32:33], v[82:83], v[82:83]
	v_pk_fma_f32 v[52:53], v[18:19], v[52:53], v[52:53]
	v_pk_fma_f32 v[26:27], v[20:21], v[26:27], v[26:27]
	v_rcp_f32_e64 v62, v62 clamp
	v_rcp_f32_e64 v63, v63 clamp
	v_rcp_f32_e64 v64, v64 clamp
	v_rcp_f32_e64 v65, v65 clamp
	v_rcp_f32_e64 v76, v76 clamp
	v_rcp_f32_e64 v77, v77 clamp
	v_rcp_f32_e64 v78, v78 clamp
	v_rcp_f32_e64 v79, v79 clamp
	v_rcp_f32_e64 v80, v80 clamp
	v_rcp_f32_e64 v81, v81 clamp
	v_rcp_f32_e64 v82, v82 clamp
	v_rcp_f32_e64 v83, v83 clamp
	v_rcp_f32_e64 v52, v52 clamp
	v_rcp_f32_e64 v53, v53 clamp
	v_rcp_f32_e64 v26, v26 clamp
	v_rcp_f32_e64 v27, v27 clamp
	v_pk_mul_f32 v[52:53], v[54:55], v[52:53]
	v_pk_mul_f32 v[0:1], v[0:1], v[62:63]
	v_pk_mul_f32 v[44:45], v[44:45], v[64:65]
	v_pk_mul_f32 v[46:47], v[46:47], v[76:77]
	v_pk_mul_f32 v[56:57], v[56:57], v[78:79]
	v_pk_mul_f32 v[62:63], v[66:67], v[80:81]
	v_pk_mul_f32 v[64:65], v[74:75], v[82:83]
	v_pk_mul_f32 v[26:27], v[28:29], v[26:27]
	v_pk_fma_f32 v[18:19], v[18:19], v[52:53], v[52:53]
	v_pk_fma_f32 v[28:29], v[48:49], v[0:1], v[0:1]
	v_pk_fma_f32 v[48:49], v[50:51], v[44:45], v[44:45]
	v_pk_fma_f32 v[50:51], v[58:59], v[46:47], v[46:47]
	v_pk_fma_f32 v[54:55], v[60:61], v[56:57], v[56:57]
	v_pk_fma_f32 v[30:31], v[30:31], v[62:63], v[62:63]
	v_pk_fma_f32 v[32:33], v[32:33], v[64:65], v[64:65]
	v_pk_fma_f32 v[20:21], v[20:21], v[26:27], v[26:27]
	v_pk_fma_f32 v[28:29], v[28:29], v[28:29], s[4:5] neg_lo:[1,0,0] neg_hi:[1,0,0] clamp
	v_pk_fma_f32 v[48:49], v[48:49], v[48:49], s[4:5] neg_lo:[1,0,0] neg_hi:[1,0,0] clamp
	v_pk_fma_f32 v[50:51], v[50:51], v[50:51], s[4:5] neg_lo:[1,0,0] neg_hi:[1,0,0] clamp
	v_pk_fma_f32 v[54:55], v[54:55], v[54:55], s[4:5] neg_lo:[1,0,0] neg_hi:[1,0,0] clamp
	v_pk_fma_f32 v[30:31], v[30:31], v[30:31], s[4:5] neg_lo:[1,0,0] neg_hi:[1,0,0] clamp
	v_pk_fma_f32 v[32:33], v[32:33], v[32:33], s[4:5] neg_lo:[1,0,0] neg_hi:[1,0,0] clamp
	v_pk_fma_f32 v[18:19], v[18:19], v[18:19], s[4:5] neg_lo:[1,0,0] neg_hi:[1,0,0] clamp
	v_pk_fma_f32 v[20:21], v[20:21], v[20:21], s[4:5] neg_lo:[1,0,0] neg_hi:[1,0,0] clamp
	v_pk_fma_f32 v[28:29], v[28:29], v[28:29], s[8:9] op_sel_hi:[1,1,0]
	v_pk_fma_f32 v[48:49], v[48:49], v[48:49], s[8:9] op_sel_hi:[1,1,0]
	v_pk_fma_f32 v[50:51], v[50:51], v[50:51], s[8:9] op_sel_hi:[1,1,0]
	v_pk_fma_f32 v[54:55], v[54:55], v[54:55], s[8:9] op_sel_hi:[1,1,0]
	v_pk_fma_f32 v[30:31], v[30:31], v[30:31], s[8:9] op_sel_hi:[1,1,0]
	v_pk_fma_f32 v[32:33], v[32:33], v[32:33], s[8:9] op_sel_hi:[1,1,0]
	v_pk_fma_f32 v[18:19], v[18:19], v[18:19], s[8:9] op_sel_hi:[1,1,0]
	v_pk_fma_f32 v[20:21], v[20:21], v[20:21], s[8:9] op_sel_hi:[1,1,0]
	v_pk_mul_f32 v[0:1], v[0:1], v[28:29]
	v_pk_mul_f32 v[58:59], v[44:45], v[48:49]
	v_pk_mul_f32 v[60:61], v[46:47], v[50:51]
	v_pk_mul_f32 v[54:55], v[56:57], v[54:55]
	v_pk_mul_f32 v[62:63], v[62:63], v[30:31]
	v_pk_mul_f32 v[64:65], v[64:65], v[32:33]
	v_pk_mul_f32 v[66:67], v[18:19], v[52:53]
	v_pk_mul_f32 v[74:75], v[26:27], v[20:21]
	ds_read_b128 v[18:21], v72 offset:36864
	ds_read_b128 v[30:33], v72 offset:37888
	ds_read_b128 v[26:29], v71 offset:43520
	v_cvt_pk_f16_f32 v56, v60, v61
	v_cvt_pk_f16_f32 v57, v54, v55
	v_cvt_pk_f16_f32 v54, v62, v63
	ds_read_b128 v[60:63], v71 offset:43584
	v_cvt_pk_f16_f32 v52, v0, v1
	v_cvt_pk_f16_f32 v53, v58, v59
	s_waitcnt lgkmcnt(1)
	v_mfma_f32_16x16x32_f16 v[48:51], v[18:21], v[34:37], v[26:29]
	v_cvt_pk_f16_f32 v55, v64, v65
	v_cvt_pk_f16_f32 v58, v66, v67
	v_mfma_f32_16x16x32_f16 v[18:21], v[18:21], v[22:25], v[26:29]
	ds_read_b128 v[44:47], v72 offset:40960
	s_add_i32 s12, s12, s3
	s_add_i32 s10, s20, s12
	v_cvt_pk_f16_f32 v59, v74, v75
	v_mfma_f32_16x16x32_f16 v[26:29], v[30:33], v[52:55], v[48:51]
	s_cmp_lt_i32 s10, 0x8000
	v_add_u32_e32 v38, s7, v38
	s_nop 0
	ds_read_b128 v[48:51], v72 offset:38912
	v_mfma_f32_16x16x32_f16 v[18:21], v[30:33], v[56:59], v[18:21]
	ds_read_b128 v[30:33], v72 offset:39936
	s_nop 1
	v_cvt_pk_f16_f32 v1, v28, v29
	v_cvt_pk_f16_f32 v0, v26, v27
	s_waitcnt lgkmcnt(1)
	v_mfma_f32_16x16x32_f16 v[34:37], v[48:51], v[34:37], v[60:63]
	v_pk_max_f16 v27, v1, 0
	v_cvt_pk_f16_f32 v1, v20, v21
	v_pk_max_f16 v26, v0, 0
	v_mfma_f32_16x16x32_f16 v[20:23], v[48:51], v[22:25], v[60:63]
	v_cvt_pk_f16_f32 v0, v18, v19
	v_pk_max_f16 v18, v0, 0
	s_waitcnt lgkmcnt(0)
	v_mfma_f32_16x16x32_f16 v[34:37], v[30:33], v[52:55], v[34:37]
	v_pk_max_f16 v19, v1, 0
	v_mfma_f32_16x16x32_f16 v[20:23], v[30:33], v[56:59], v[20:23]
	s_nop 6
	v_cvt_pk_f16_f32 v0, v34, v35
	v_cvt_pk_f16_f32 v1, v36, v37
	v_pk_max_f16 v28, v0, 0
	v_pk_max_f16 v29, v1, 0
	v_cvt_pk_f16_f32 v0, v20, v21
	v_cvt_pk_f16_f32 v1, v22, v23
	v_pk_max_f16 v20, v0, 0
	v_mfma_f32_16x16x32_f16 v[24:27], v[44:47], v[26:29], 0
	v_pk_max_f16 v21, v1, 0
	s_nop 1
	v_mfma_f32_16x16x32_f16 v[18:21], v[44:47], v[18:21], 0
	s_nop 7
	v_cndmask_b32_e64 v18, v24, v18, s[0:1]
	s_cbranch_scc0 .LBB0_37
